# chain DMA prefetch ahead of scattered loads + phase P: counted waits so store acks are not waited for (unit top, q/k use)
# speedup vs baseline: 1.0137x; 1.0058x over previous
; #define GAS __attribute__((address_space(1)))
; #define LAS __attribute__((address_space(3)))
; DI int rfl(int v) { return __builtin_amdgcn_readfirstlane(v); }
; DI int ltid() { int t = threadIdx.x; asm volatile("" : "+v"(t)); return t; }
; DI bf16_t* wsb(const Ctx& c, size_t off) { return (bf16_t*)(c.ws + off); }
; DI void gla_p_unit(LAS unsigned char* lds, const Ctx& c, int l, int bl, int h, int n, int& h_loaded) {
;     const int tid = ltid(), lane = tid & 63, w = rfl(tid >> 6), fr = lane & 15, fq = lane >> 4;
;     const size_t tok0 = (size_t)bl * SEQ + n * 64;
;     const bf16_t* QG = wsb(c, WS_H + H_QG) + tok0 * 512 + h * 128;
;     const bf16_t* KG = wsb(c, WS_H + H_KG) + tok0 * 512 + h * 128;
;     const bf16_t* VG = wsb(c, WS_H + H_VG) + tok0 * 1024 + h * 256;
;     const float* HA = (const float*)(c.ws + WS_HA) + tok0 * 16;
;     const int unit = (bl * 4 + h) * 64 + n;
;     unsigned char* rec = c.ws + WS_REC + (size_t)unit * REC_BYTES;
;     unsigned char* oi = c.ws + WS_MIX + (size_t)unit * OI_BYTES;
;     LAS bf16_t* QT = (LAS bf16_t*)(lds + GP_QT); LAS bf16_t* KT = (LAS bf16_t*)(lds + GP_KT); LAS bf16_t* VS = (LAS bf16_t*)(lds + GP_VS); LAS bf16_t* AT = (LAS bf16_t*)(lds + GP_ATT);
;     LAS float* WUP = (LAS float*)(lds + GP_WUP); LAS float* BAL = (LAS float*)(lds + GP_BAL);
;     __syncthreads();
;     if (h_loaded != h) { for (int i = tid; i < 16 * 128; i += NTHREADS) WUP[i] = ((const GAS float*)c.w_alpha_up)[(size_t)l * 16 * 512 + (i >> 7) * 512 + h * 128 + (i & 127)];
;         if (tid < 128) BAL[tid] = ((const GAS float*)c.b_alpha)[l * 512 + h * 128 + tid]; h_loaded = h; __syncthreads(); }
.LBB0_564:
	s_bfe_u32 s6, s38, 0x20006
	s_nop 0
	v_mov_b32_e32 v2, v0
	s_lshl_b32 s7, s6, 7
	s_cmp_eq_u32 s63, s6
	v_readfirstlane_b32 s67, v2
	s_barrier
	s_cbranch_scc1 .LBB0_576
	s_movk_i32 s8, 0x800
	v_cmp_gt_i32_e32 vcc, s8, v2
	s_and_saveexec_b64 s[30:31], vcc
	s_cbranch_execz .LBB0_573
	v_and_b32_e32 v1, 0x7f, v2
	v_lshlrev_b32_e32 v6, 2, v1
	v_max_i32_e32 v1, 0x600, v2
	v_mov_b32_e32 v7, v4
	v_sub_u32_e32 v1, v1, v2
	v_lshl_add_u64 v[6:7], s[16:17], 0, v[6:7]
	s_lshl_b32 s68, s7, 2
	v_add_u32_e32 v1, 0x1ff, v1
	s_movk_i32 s8, 0x1ff
	v_lshl_add_u64 v[6:7], v[6:7], 0, s[68:69]
	v_cmp_lt_u32_e32 vcc, s8, v1
	s_mov_b64 s[44:45], -1
	v_mov_b32_e32 v3, v2
	s_and_saveexec_b64 s[40:41], vcc
	s_cbranch_execz .LBB0_570
	v_lshrrev_b32_e32 v1, 9, v1
	v_add_u32_e32 v1, 1, v1
	v_and_b32_e32 v5, 0xfffffe, v1
	v_add_u32_e32 v3, 0x200, v2
	v_lshl_add_u32 v10, v2, 2, s62
	s_mov_b64 s[44:45], 0
	v_mov_b32_e32 v11, v5
	v_mov_b64_e32 v[8:9], v[2:3]

; DI float exp_(float x) { return __builtin_amdgcn_exp2f(x * LOG2E); }
; DI void unpack8(const u32x4& q, float (&v)[16], int o) { v[o] = bf_lo(q.x); v[o + 1] = bf_hi(q.x); v[o + 2] = bf_lo(q.y); v[o + 3] = bf_hi(q.y); v[o + 4] = bf_lo(q.z); v[o + 5] = bf_hi(q.z); v[o + 6] = bf_lo(q.w); v[o + 7] = bf_hi(q.w); }
; DI void gla_p_unit(LAS unsigned char* lds, const Ctx& c, int l, int bl, int h, int n, int& h_loaded) {
;     ...
; #pragma unroll
;         for (int cc = 0; cc < 16; ++cc) { const float z = la[cc]; la[cc] = -(fmaxf(-z, 0.f) + __builtin_amdgcn_logf(1.0f + exp_(-fabsf(z))) * 0.6931471805599453f) * (1.0f / 16.0f); }
; #pragma unroll
;         for (int cc = 0; cc < 16; ++cc) la[cc] = scan64(la[cc]);
;         float qv[16], kv[16];
;         unpack8(q0, qv, 0); unpack8(q1, qv, 8); unpack8(k0, kv, 0); unpack8(k1, kv, 8);
;         float dc[16];
; #pragma unroll
;         for (int cc = 0; cc < 16; ++cc) { const float b = la[cc]; const float bend = __shfl(b, 63); const float eb = exp_(b); dc[cc] = eb; qv[cc] *= eb; la[cc] = kv[cc] * exp_(bend - b); kv[cc] *= exp_(-b); }
.LBB0_578:
	s_or_b64 exec, exec, s[46:47]
	s_waitcnt lgkmcnt(14)
	v_sub_f32_e32 v67, v67, v3
	v_mul_f32_e32 v3, 0xbfb8aa3b, v3
	v_exp_f32_e32 v78, v3
	v_sub_f32_e32 v3, v66, v39
	v_mul_f32_e32 v67, 0x3fb8aa3b, v67
	v_mul_f32_e32 v3, 0x3fb8aa3b, v3
	v_mul_f32_e32 v39, 0xbfb8aa3b, v39
	v_exp_f32_e32 v76, v67
	v_exp_f32_e32 v79, v39
	v_exp_f32_e32 v77, v3
	s_waitcnt lgkmcnt(13)
	v_sub_f32_e32 v3, v65, v5
	s_waitcnt vmcnt(6)
	v_lshlrev_b32_e32 v68, 16, v18
	v_and_b32_e32 v69, 0xffff0000, v18
	s_waitcnt vmcnt(4)
	v_lshlrev_b32_e32 v66, 16, v10
	v_and_b32_e32 v67, 0xffff0000, v10
	v_mul_f32_e32 v3, 0x3fb8aa3b, v3
	v_pk_mul_f32 v[34:35], v[34:35], v[68:69]
	v_pk_mul_f32 v[68:69], v[78:79], v[66:67]
	v_pk_mul_f32 v[66:67], v[76:77], v[66:67]
	v_exp_f32_e32 v76, v3
	v_mul_f32_e32 v3, 0xbfb8aa3b, v5
	v_exp_f32_e32 v78, v3
	s_waitcnt lgkmcnt(12)
	v_sub_f32_e32 v3, v64, v41
	v_mul_f32_e32 v3, 0x3fb8aa3b, v3
	v_mul_f32_e32 v5, 0xbfb8aa3b, v41
	v_exp_f32_e32 v79, v5
	v_exp_f32_e32 v77, v3
	s_waitcnt lgkmcnt(11)
	v_sub_f32_e32 v3, v63, v38
	v_lshlrev_b32_e32 v18, 16, v19
	v_and_b32_e32 v19, 0xffff0000, v19
	v_lshlrev_b32_e32 v10, 16, v11
	v_and_b32_e32 v11, 0xffff0000, v11
	v_mul_f32_e32 v3, 0x3fb8aa3b, v3
	v_pk_mul_f32 v[18:19], v[36:37], v[18:19]
	v_pk_mul_f32 v[36:37], v[78:79], v[10:11]
	v_pk_mul_f32 v[64:65], v[76:77], v[10:11]
	v_exp_f32_e32 v10, v3
	v_mul_f32_e32 v3, 0xbfb8aa3b, v38
	v_exp_f32_e32 v38, v3
	s_waitcnt lgkmcnt(10)
	v_sub_f32_e32 v3, v62, v43
	v_mul_f32_e32 v3, 0x3fb8aa3b, v3
	v_mul_f32_e32 v5, 0xbfb8aa3b, v43
	v_exp_f32_e32 v39, v5
	v_exp_f32_e32 v11, v3
	s_waitcnt lgkmcnt(9)
	v_sub_f32_e32 v3, v61, v40
	v_lshlrev_b32_e32 v62, 16, v12
	v_and_b32_e32 v63, 0xffff0000, v12
	v_mul_f32_e32 v3, 0x3fb8aa3b, v3
	v_pk_mul_f32 v[38:39], v[38:39], v[62:63]
	v_pk_mul_f32 v[62:63], v[10:11], v[62:63]
	v_exp_f32_e32 v10, v3
	v_mul_f32_e32 v3, 0xbfb8aa3b, v40
	v_exp_f32_e32 v40, v3
	s_waitcnt lgkmcnt(8)
	v_sub_f32_e32 v3, v60, v45
	v_mul_f32_e32 v3, 0x3fb8aa3b, v3
	v_mul_f32_e32 v5, 0xbfb8aa3b, v45
	v_exp_f32_e32 v41, v5
	v_exp_f32_e32 v11, v3
	s_waitcnt lgkmcnt(7)
	v_sub_f32_e32 v3, v59, v42
	v_lshlrev_b32_e32 v70, 16, v20
	v_and_b32_e32 v71, 0xffff0000, v20
	v_lshlrev_b32_e32 v20, 16, v21
	v_and_b32_e32 v21, 0xffff0000, v21
	v_lshlrev_b32_e32 v12, 16, v13
	v_and_b32_e32 v13, 0xffff0000, v13
	v_mul_f32_e32 v3, 0x3fb8aa3b, v3
	v_pk_mul_f32 v[20:21], v[32:33], v[20:21]
	v_pk_mul_f32 v[32:33], v[40:41], v[12:13]
	v_pk_mul_f32 v[40:41], v[10:11], v[12:13]
	v_exp_f32_e32 v10, v3
	v_mul_f32_e32 v3, 0xbfb8aa3b, v42
	v_exp_f32_e32 v12, v3
	s_waitcnt lgkmcnt(6)
	v_sub_f32_e32 v3, v58, v47
	v_mul_f32_e32 v3, 0x3fb8aa3b, v3
	v_mul_f32_e32 v5, 0xbfb8aa3b, v47
	v_exp_f32_e32 v13, v5
	v_exp_f32_e32 v11, v3
	s_waitcnt lgkmcnt(5)
	v_sub_f32_e32 v3, v57, v44
	v_lshlrev_b32_e32 v42, 16, v6
	v_and_b32_e32 v43, 0xffff0000, v6
	v_mul_f32_e32 v3, 0x3fb8aa3b, v3
	v_pk_mul_f32 v[58:59], v[12:13], v[42:43]
	v_pk_mul_f32 v[42:43], v[10:11], v[42:43]
	v_exp_f32_e32 v10, v3
	v_mul_f32_e32 v3, 0xbfb8aa3b, v44
	v_exp_f32_e32 v12, v3
	s_waitcnt lgkmcnt(4)
	v_sub_f32_e32 v3, v56, v49
	v_mul_f32_e32 v3, 0x3fb8aa3b, v3
	v_mul_f32_e32 v5, 0xbfb8aa3b, v49
	v_exp_f32_e32 v13, v5
	v_exp_f32_e32 v11, v3
	s_waitcnt lgkmcnt(3)
	v_sub_f32_e32 v3, v55, v46
	v_lshlrev_b32_e32 v72, 16, v14
	v_and_b32_e32 v73, 0xffff0000, v14
	v_lshlrev_b32_e32 v14, 16, v15
	v_and_b32_e32 v15, 0xffff0000, v15
	v_lshlrev_b32_e32 v6, 16, v7
	v_and_b32_e32 v7, 0xffff0000, v7
	v_mul_f32_e32 v3, 0x3fb8aa3b, v3
	v_pk_mul_f32 v[14:15], v[28:29], v[14:15]
	v_pk_mul_f32 v[28:29], v[12:13], v[6:7]
	v_pk_mul_f32 v[44:45], v[10:11], v[6:7]
	v_exp_f32_e32 v6, v3
	v_mul_f32_e32 v3, 0xbfb8aa3b, v46
	v_exp_f32_e32 v10, v3
	s_waitcnt lgkmcnt(2)
	v_sub_f32_e32 v3, v54, v50
	v_mul_f32_e32 v3, 0x3fb8aa3b, v3
	v_mul_f32_e32 v5, 0xbfb8aa3b, v50
	v_exp_f32_e32 v7, v3
	v_exp_f32_e32 v11, v5
	v_lshlrev_b32_e32 v74, 16, v16
	v_and_b32_e32 v75, 0xffff0000, v16
	s_waitcnt lgkmcnt(1)
; #define GAS __attribute__((address_space(1)))
; #define LAS __attribute__((address_space(3)))
; #define MFMA16(a, b, c) __builtin_amdgcn_mfma_f32_16x16x32_bf16((a), (b), (c), 0, 0, 0)
; DI float exp_(float x) { return __builtin_amdgcn_exp2f(x * LOG2E); }
; DI u32x4 packf8(const float (&v)[16], int o) { u32x4 p; p.x = cvt_pk_bf16(v[o], v[o + 1]); p.y = cvt_pk_bf16(v[o + 2], v[o + 3]); p.z = cvt_pk_bf16(v[o + 4], v[o + 5]); p.w = cvt_pk_bf16(v[o + 6], v[o + 7]); return p; }
; DI void gla_p_unit(LAS unsigned char* lds, const Ctx& c, int l, int bl, int h, int n, int& h_loaded) {
;     ...
;         for (int cc = 0; cc < 16; ++cc) { const float b = la[cc]; const float bend = __shfl(b, 63); const float eb = exp_(b); dc[cc] = eb; qv[cc] *= eb; la[cc] = kv[cc] * exp_(bend - b); kv[cc] *= exp_(-b); }
;         if (lane == 63) {
; #pragma unroll
;             for (int c4 = 0; c4 < 4; ++c4) *(GAS f32x4*)(rec + REC_DEC + (16 * w + 4 * c4) * 4) = (f32x4){dc[4 * c4], dc[4 * c4 + 1], dc[4 * c4 + 2], dc[4 * c4 + 3]}; }
;         const u32x4 qa = packf8(qv, 0), qb = packf8(qv, 8), ka = packf8(kv, 0), kb = packf8(kv, 8), sa = packf8(la, 0), sb = packf8(la, 8);
;         *(LAS u32x4*)(QT + row * 136 + 16 * w) = qa; *(LAS u32x4*)(QT + row * 136 + 16 * w + 8) = qb;
;         *(LAS u32x4*)(KT + row * 136 + 16 * w) = ka; *(LAS u32x4*)(KT + row * 136 + 16 * w + 8) = kb;
;         *(GAS u32x4*)(rec + row * 256 + (((2 * w) ^ (row & 15)) << 4)) = qa; *(GAS u32x4*)(rec + row * 256 + (((2 * w + 1) ^ (row & 15)) << 4)) = qb;
;         *(GAS u32x4*)(rec + REC_KS + row * 256 + (((2 * w) ^ (2 * (row & 7))) << 4)) = sa; *(GAS u32x4*)(rec + REC_KS + row * 256 + (((2 * w + 1) ^ (2 * (row & 7))) << 4)) = sb;
;     }
;     __syncthreads();
; #pragma unroll
;     for (int rep = 0; rep < 2; ++rep) {
;         const int tt = w + 8 * rep, jt = tt >> 2, it = tt & 3;
;         f32x4 a = (f32x4){0.f, 0.f, 0.f, 0.f};
;         if (jt <= it) {
; #pragma unroll
;             for (int k4 = 0; k4 < 4; ++k4) { const bf16x8 af = *(const LAS bf16x8*)(KT + (16 * jt + fr) * 136 + 32 * k4 + 8 * fq), bfr = *(const LAS bf16x8*)(QT + (16 * it + fr) * 136 + 32 * k4 + 8 * fq); a = MFMA16(af, bfr, a); }
	v_sub_f32_e32 v3, v53, v48
	v_pk_mul_f32 v[12:13], v[22:23], v[74:75]
	v_lshlrev_b32_e32 v22, 16, v8
	v_and_b32_e32 v23, 0xffff0000, v8
	v_mul_f32_e32 v3, 0x3fb8aa3b, v3
	v_pk_mul_f32 v[54:55], v[6:7], v[22:23]
	v_exp_f32_e32 v6, v3
	v_mul_f32_e32 v3, 0xbfb8aa3b, v48
	v_pk_mul_f32 v[46:47], v[10:11], v[22:23]
	v_exp_f32_e32 v10, v3
	s_waitcnt lgkmcnt(0)
	v_sub_f32_e32 v3, v52, v51
	v_mul_f32_e32 v3, 0x3fb8aa3b, v3
	v_mul_f32_e32 v5, 0xbfb8aa3b, v51
	v_exp_f32_e32 v11, v5
	v_exp_f32_e32 v7, v3
	s_lshl_b32 s6, s44, 1
	v_lshlrev_b32_e32 v16, 16, v17
	v_and_b32_e32 v17, 0xffff0000, v17
	v_pk_mul_f32 v[30:31], v[30:31], v[70:71]
	v_lshlrev_b32_e32 v8, 16, v9
	v_and_b32_e32 v9, 0xffff0000, v9
	v_mul_u32_u24_e32 v5, 0x88, v1
	s_add_i32 s6, s6, s5
	v_pk_mul_f32 v[26:27], v[26:27], v[72:73]
	v_pk_mul_f32 v[16:17], v[24:25], v[16:17]
	v_pk_mul_f32 v[22:23], v[10:11], v[8:9]
	v_pk_mul_f32 v[48:49], v[6:7], v[8:9]
	v_cvt_pk_bf16_f32 v6, v34, v35
	v_cvt_pk_bf16_f32 v7, v18, v19
	v_cvt_pk_bf16_f32 v8, v30, v31
	v_cvt_pk_bf16_f32 v9, v20, v21
	v_lshl_add_u32 v5, v5, 1, s6
	s_lshl_b32 s6, s66, 1
	v_cvt_pk_bf16_f32 v10, v26, v27
	v_cvt_pk_bf16_f32 v11, v14, v15
	v_cvt_pk_bf16_f32 v12, v12, v13
	v_cvt_pk_bf16_f32 v13, v16, v17
	v_cvt_pk_bf16_f32 v14, v68, v69
	v_cvt_pk_bf16_f32 v15, v36, v37
	v_cvt_pk_bf16_f32 v16, v38, v39
	v_cvt_pk_bf16_f32 v17, v32, v33
	v_cvt_pk_bf16_f32 v18, v58, v59
	v_cvt_pk_bf16_f32 v19, v28, v29
	v_cvt_pk_bf16_f32 v20, v46, v47
	v_cvt_pk_bf16_f32 v21, v22, v23
	ds_write_b128 v5, v[6:9]
	ds_write_b128 v5, v[10:13] offset:16
	ds_write_b128 v5, v[14:17] offset:17408
	ds_write_b128 v5, v[18:21] offset:17424
	v_bitop3_b32 v5, s6, v2, 15 bitop3:0x78
	v_lshlrev_b32_e32 v14, 8, v1
	v_mov_b32_e32 v15, v4
	v_lshlrev_b32_e32 v16, 4, v5
	v_and_b32_e32 v3, 15, v2
	v_lshl_add_u64 v[14:15], s[40:41], 0, v[14:15]
	v_ashrrev_i32_e32 v17, 31, v16
	v_lshl_add_u64 v[16:17], v[14:15], 0, v[16:17]
	v_bitop3_b32 v5, s6, v3, 1 bitop3:0x36
	global_store_dwordx4 v[16:17], v[6:9], off
	v_cvt_pk_bf16_f32 v22, v66, v67
	v_cvt_pk_bf16_f32 v23, v64, v65
	v_lshlrev_b32_e32 v6, 4, v5
	v_ashrrev_i32_e32 v7, 31, v6
	v_lshl_add_u64 v[6:7], v[14:15], 0, v[6:7]
	v_lshlrev_b32_e32 v5, 1, v2
	global_store_dwordx4 v[6:7], v[10:13], off
	v_lshl_add_u64 v[6:7], v[14:15], 0, s[72:73]
	v_cvt_pk_bf16_f32 v24, v62, v63
	v_and_b32_e32 v10, 14, v5
	v_bitop3_b32 v5, s6, v5, 14 bitop3:0x78
	v_lshlrev_b32_e32 v8, 4, v5
	v_ashrrev_i32_e32 v9, 31, v8
	v_cvt_pk_bf16_f32 v25, v40, v41
	v_lshl_add_u64 v[8:9], v[6:7], 0, v[8:9]
	v_bitop3_b32 v5, s6, v10, 1 bitop3:0x36
	global_store_dwordx4 v[8:9], v[22:25], off
	v_lshlrev_b32_e32 v8, 4, v5
	v_ashrrev_i32_e32 v9, 31, v8
	v_cvt_pk_bf16_f32 v26, v42, v43
	v_cvt_pk_bf16_f32 v27, v44, v45
	v_cvt_pk_bf16_f32 v28, v54, v55
	v_cvt_pk_bf16_f32 v29, v48, v49
	v_lshl_add_u64 v[6:7], v[6:7], 0, v[8:9]
	global_store_dwordx4 v[6:7], v[26:29], off
	s_bfe_u32 s6, s67, 0x20006
	v_and_b32_e32 v6, 48, v1
	v_lshl_or_b32 v5, s6, 4, v3
	v_add_u32_e32 v12, s5, v6
	s_movk_i32 s7, 0x110
	s_ashr_i32 s8, s67, 8
	v_mad_u32_u24 v13, v5, s7, v12
	s_lshl_b32 s7, s8, 4
	s_cmp_gt_i32 s8, s6
	v_mov_b32_e32 v6, 0
	v_mov_b32_e32 v8, 0
	v_mov_b32_e32 v9, 0
	v_mov_b32_e32 v10, 0
	v_mov_b32_e32 v11, 0
	s_waitcnt lgkmcnt(0)
	s_barrier
	s_cbranch_scc1 .LBB0_580
	v_or_b32_e32 v7, s7, v3
	s_movk_i32 s8, 0x110
	v_mad_u64_u32 v[22:23], s[8:9], v7, s8, v[12:13]
	ds_read_b128 v[8:11], v22 offset:17408
	ds_read_b128 v[14:17], v13
	s_waitcnt lgkmcnt(0)
	v_mfma_f32_16x16x32_bf16 v[8:11], v[8:11], v[14:17], 0
	ds_read_b128 v[14:17], v22 offset:17472
	ds_read_b128 v[18:21], v13 offset:64
	s_waitcnt lgkmcnt(0)
	v_mfma_f32_16x16x32_bf16 v[8:11], v[14:17], v[18:21], v[8:11]
	ds_read_b128 v[14:17], v22 offset:17536
	ds_read_b128 v[18:21], v13 offset:128
	s_waitcnt lgkmcnt(0)
	v_mfma_f32_16x16x32_bf16 v[8:11], v[14:17], v[18:21], v[8:11]
	ds_read_b128 v[14:17], v22 offset:17600
	ds_read_b128 v[18:21], v13 offset:192
	s_waitcnt lgkmcnt(0)
	v_mfma_f32_16x16x32_bf16 v[8:11], v[14:17], v[18:21], v[8:11]
